# HGRN scan: all 64 loads of an item issued up front, serial fma chain after (plus barrier changes)
# baseline (speedup 1.0000x reference)
; #define GAS __attribute__((address_space(1)))
; #define SB() __builtin_amdgcn_sched_barrier(0)
; __device__ __forceinline__ unsigned cvt_pk_bf16(float lo, float hi) { unsigned r; asm volatile("v_cvt_pk_bf16_f32 %0, %1, %2" : "=v"(r) : "v"(lo), "v"(hi)); return r; }
; __device__ __forceinline__ float bflo(unsigned w) { return __uint_as_float(w << 16); }
; __device__ __forceinline__ float bfhi(unsigned w) { return __uint_as_float(w & 0xffff0000u); }
; __device__ __forceinline__ void hg_scan_item(Frame& F, int B) {
;     const int bh = B >> 4, e2 = (B & 15) * 512 + F.tid, d = (2 * e2) & 127;
;     const unsigned* ut = WSP(unsigned, WS_UT) + (size_t)bh * 32 * 8192 + e2; const float* gd = WSP(float, WS_GD) + (size_t)bh * 32 * 128 + d;
;     unsigned* sp = WSP(unsigned, WS_SPT) + (size_t)bh * 32 * 8192 + e2;
;     float s0 = 0.f, s1 = 0.f;
; #pragma unroll 1
;     for (int c0 = 0; c0 < 32; c0 += 8) { unsigned u[8]; f32x2 gg[8];
; #pragma unroll
;         for (int i = 0; i < 8; ++i) { u[i] = ut[(size_t)(c0 + i) * 8192]; gg[i] = *(const GAS f32x2*)(gd + (c0 + i) * 128); }
;         SB();
; #pragma unroll
;         for (int i = 0; i < 8; ++i) { sp[(size_t)(c0 + i) * 8192] = cvt_pk_bf16(s0, s1); s0 = gg[i].x * s0 + bflo(u[i]); s1 = gg[i].y * s1 + bfhi(u[i]); } }
.LBB0_777:
	s_and_b32 s8, s6, 0x1e00
	v_add_u32_e32 v4, s8, v204
	s_ashr_i32 s8, s7, 4
	s_ashr_i32 s9, s8, 31
	s_lshl_b64 s[10:11], s[8:9], 14
	s_lshl_b64 s[8:9], s[8:9], 20
	s_add_u32 s8, s90, s8
	v_ashrrev_i32_e32 v5, 31, v4
	s_addc_u32 s9, s91, s9
	v_mov_b32_e32 v10, 0
	v_lshl_add_u64 v[4:5], v[4:5], 2, s[8:9]
	v_lshl_add_u64 v[6:7], v[2:3], 0, s[10:11]
	s_mov_b32 s8, -8
	v_mov_b32_e32 v11, v10
	v_lshl_add_u64 v[8:9], v[4:5], 0, s[4:5]
	v_lshl_add_u64 v[12:13], v[6:7], 0, s[4:5]
	s_mov_b64 s[10:11], 0x8000
	v_add_co_u32_e32 v14, vcc, 0x2ae41000, v8
	s_nop 1
	v_addc_co_u32_e32 v15, vcc, 0, v9, vcc
	v_add_co_u32_e32 v18, vcc, 0x2ce81000, v8
	s_nop 1
	v_addc_co_u32_e32 v19, vcc, 0, v9, vcc
	global_load_dword v40, v[14:15], off
	global_load_dwordx2 v[72:73], v[12:13], off offset:-2048
	v_lshl_add_u64 v[14:15], v[14:15], 0, s[10:11]
	global_load_dword v41, v[14:15], off
	global_load_dwordx2 v[74:75], v[12:13], off offset:-1536
	v_lshl_add_u64 v[14:15], v[14:15], 0, s[10:11]
	global_load_dword v42, v[14:15], off
	global_load_dwordx2 v[76:77], v[12:13], off offset:-1024
	v_lshl_add_u64 v[14:15], v[14:15], 0, s[10:11]
	global_load_dword v43, v[14:15], off
	global_load_dwordx2 v[78:79], v[12:13], off offset:-512
	v_lshl_add_u64 v[14:15], v[14:15], 0, s[10:11]
	global_load_dword v44, v[14:15], off
	global_load_dwordx2 v[80:81], v[12:13], off
	v_lshl_add_u64 v[14:15], v[14:15], 0, s[10:11]
	global_load_dword v45, v[14:15], off
	global_load_dwordx2 v[82:83], v[12:13], off offset:512
	v_lshl_add_u64 v[14:15], v[14:15], 0, s[10:11]
	global_load_dword v46, v[14:15], off
	global_load_dwordx2 v[84:85], v[12:13], off offset:1024
	v_lshl_add_u64 v[14:15], v[14:15], 0, s[10:11]
	global_load_dword v47, v[14:15], off
	global_load_dwordx2 v[86:87], v[12:13], off offset:1536
	v_lshl_add_u64 v[14:15], v[14:15], 0, s[10:11]
	v_lshl_add_u64 v[12:13], v[12:13], 0, s[30:31]
	global_load_dword v48, v[14:15], off
	global_load_dwordx2 v[88:89], v[12:13], off offset:-2048
	v_lshl_add_u64 v[14:15], v[14:15], 0, s[10:11]
	global_load_dword v49, v[14:15], off
	global_load_dwordx2 v[90:91], v[12:13], off offset:-1536
	v_lshl_add_u64 v[14:15], v[14:15], 0, s[10:11]
	global_load_dword v50, v[14:15], off
	global_load_dwordx2 v[92:93], v[12:13], off offset:-1024
	v_lshl_add_u64 v[14:15], v[14:15], 0, s[10:11]
	global_load_dword v51, v[14:15], off
	global_load_dwordx2 v[94:95], v[12:13], off offset:-512
	v_lshl_add_u64 v[14:15], v[14:15], 0, s[10:11]
	global_load_dword v52, v[14:15], off
	global_load_dwordx2 v[96:97], v[12:13], off
	v_lshl_add_u64 v[14:15], v[14:15], 0, s[10:11]
	global_load_dword v53, v[14:15], off
	global_load_dwordx2 v[98:99], v[12:13], off offset:512
	v_lshl_add_u64 v[14:15], v[14:15], 0, s[10:11]
	global_load_dword v54, v[14:15], off
	global_load_dwordx2 v[100:101], v[12:13], off offset:1024
	v_lshl_add_u64 v[14:15], v[14:15], 0, s[10:11]
	global_load_dword v55, v[14:15], off
	global_load_dwordx2 v[102:103], v[12:13], off offset:1536
	v_lshl_add_u64 v[14:15], v[14:15], 0, s[10:11]
	v_lshl_add_u64 v[12:13], v[12:13], 0, s[30:31]
	global_load_dword v56, v[14:15], off
	global_load_dwordx2 v[104:105], v[12:13], off offset:-2048
	v_lshl_add_u64 v[14:15], v[14:15], 0, s[10:11]
	global_load_dword v57, v[14:15], off
	global_load_dwordx2 v[106:107], v[12:13], off offset:-1536
	v_lshl_add_u64 v[14:15], v[14:15], 0, s[10:11]
	global_load_dword v58, v[14:15], off
	global_load_dwordx2 v[108:109], v[12:13], off offset:-1024
	v_lshl_add_u64 v[14:15], v[14:15], 0, s[10:11]
	global_load_dword v59, v[14:15], off
	global_load_dwordx2 v[110:111], v[12:13], off offset:-512
	v_lshl_add_u64 v[14:15], v[14:15], 0, s[10:11]
	global_load_dword v60, v[14:15], off
	global_load_dwordx2 v[112:113], v[12:13], off
	v_lshl_add_u64 v[14:15], v[14:15], 0, s[10:11]
	global_load_dword v61, v[14:15], off
	global_load_dwordx2 v[114:115], v[12:13], off offset:512
	v_lshl_add_u64 v[14:15], v[14:15], 0, s[10:11]
	global_load_dword v62, v[14:15], off
	global_load_dwordx2 v[116:117], v[12:13], off offset:1024
	v_lshl_add_u64 v[14:15], v[14:15], 0, s[10:11]
	global_load_dword v63, v[14:15], off
	global_load_dwordx2 v[118:119], v[12:13], off offset:1536
	v_lshl_add_u64 v[14:15], v[14:15], 0, s[10:11]
	v_lshl_add_u64 v[12:13], v[12:13], 0, s[30:31]
	global_load_dword v64, v[14:15], off
	global_load_dwordx2 v[120:121], v[12:13], off offset:-2048
	v_lshl_add_u64 v[14:15], v[14:15], 0, s[10:11]
	global_load_dword v65, v[14:15], off
	global_load_dwordx2 v[122:123], v[12:13], off offset:-1536
	v_lshl_add_u64 v[14:15], v[14:15], 0, s[10:11]
	global_load_dword v66, v[14:15], off
	global_load_dwordx2 v[124:125], v[12:13], off offset:-1024
	v_lshl_add_u64 v[14:15], v[14:15], 0, s[10:11]
	global_load_dword v67, v[14:15], off
	global_load_dwordx2 v[126:127], v[12:13], off offset:-512
	v_lshl_add_u64 v[14:15], v[14:15], 0, s[10:11]
	global_load_dword v68, v[14:15], off
	global_load_dwordx2 v[128:129], v[12:13], off
	v_lshl_add_u64 v[14:15], v[14:15], 0, s[10:11]
	global_load_dword v69, v[14:15], off
	global_load_dwordx2 v[130:131], v[12:13], off offset:512
	v_lshl_add_u64 v[14:15], v[14:15], 0, s[10:11]
	global_load_dword v70, v[14:15], off
	global_load_dwordx2 v[132:133], v[12:13], off offset:1024
	v_lshl_add_u64 v[14:15], v[14:15], 0, s[10:11]
	global_load_dword v71, v[14:15], off
	global_load_dwordx2 v[134:135], v[12:13], off offset:1536
	v_cvt_pk_bf16_f32 v0, v10, v11
	s_waitcnt vmcnt(62)
	global_store_dword v[18:19], v0, off
	v_lshlrev_b32_e32 v20, 16, v40
	v_and_b32_e32 v21, 0xffff0000, v40
	v_lshl_add_u64 v[18:19], v[18:19], 0, s[10:11]
	v_pk_fma_f32 v[10:11], v[10:11], v[72:73], v[20:21]
	v_cvt_pk_bf16_f32 v0, v10, v11
	s_waitcnt vmcnt(61)
; #define GAS __attribute__((address_space(1)))
; #define SB() __builtin_amdgcn_sched_barrier(0)
; __device__ __forceinline__ unsigned cvt_pk_bf16(float lo, float hi) { unsigned r; asm volatile("v_cvt_pk_bf16_f32 %0, %1, %2" : "=v"(r) : "v"(lo), "v"(hi)); return r; }
; __device__ __forceinline__ float bflo(unsigned w) { return __uint_as_float(w << 16); }
; __device__ __forceinline__ float bfhi(unsigned w) { return __uint_as_float(w & 0xffff0000u); }
; __device__ __forceinline__ void hg_scan_item(Frame& F, int B) {
;     ...
;     for (int c0 = 0; c0 < 32; c0 += 8) { unsigned u[8]; f32x2 gg[8];
; #pragma unroll
;         for (int i = 0; i < 8; ++i) { u[i] = ut[(size_t)(c0 + i) * 8192]; gg[i] = *(const GAS f32x2*)(gd + (c0 + i) * 128); }
;         SB();
; #pragma unroll
;         for (int i = 0; i < 8; ++i) { sp[(size_t)(c0 + i) * 8192] = cvt_pk_bf16(s0, s1); s0 = gg[i].x * s0 + bflo(u[i]); s1 = gg[i].y * s1 + bfhi(u[i]); } }
	global_store_dword v[18:19], v0, off
	v_lshlrev_b32_e32 v20, 16, v41
	v_and_b32_e32 v21, 0xffff0000, v41
	v_lshl_add_u64 v[18:19], v[18:19], 0, s[10:11]
	v_pk_fma_f32 v[10:11], v[10:11], v[74:75], v[20:21]
	v_cvt_pk_bf16_f32 v0, v10, v11
	s_waitcnt vmcnt(60)
	global_store_dword v[18:19], v0, off
	v_lshlrev_b32_e32 v20, 16, v42
	v_and_b32_e32 v21, 0xffff0000, v42
	v_lshl_add_u64 v[18:19], v[18:19], 0, s[10:11]
	v_pk_fma_f32 v[10:11], v[10:11], v[76:77], v[20:21]
	v_cvt_pk_bf16_f32 v0, v10, v11
	s_waitcnt vmcnt(59)
	global_store_dword v[18:19], v0, off
	v_lshlrev_b32_e32 v20, 16, v43
	v_and_b32_e32 v21, 0xffff0000, v43
	v_lshl_add_u64 v[18:19], v[18:19], 0, s[10:11]
	v_pk_fma_f32 v[10:11], v[10:11], v[78:79], v[20:21]
	v_cvt_pk_bf16_f32 v0, v10, v11
	s_waitcnt vmcnt(58)
	global_store_dword v[18:19], v0, off
	v_lshlrev_b32_e32 v20, 16, v44
	v_and_b32_e32 v21, 0xffff0000, v44
	v_lshl_add_u64 v[18:19], v[18:19], 0, s[10:11]
	v_pk_fma_f32 v[10:11], v[10:11], v[80:81], v[20:21]
	v_cvt_pk_bf16_f32 v0, v10, v11
	s_waitcnt vmcnt(57)
	global_store_dword v[18:19], v0, off
	v_lshlrev_b32_e32 v20, 16, v45
	v_and_b32_e32 v21, 0xffff0000, v45
	v_lshl_add_u64 v[18:19], v[18:19], 0, s[10:11]
	v_pk_fma_f32 v[10:11], v[10:11], v[82:83], v[20:21]
	v_cvt_pk_bf16_f32 v0, v10, v11
	s_waitcnt vmcnt(56)
	global_store_dword v[18:19], v0, off
	v_lshlrev_b32_e32 v20, 16, v46
	v_and_b32_e32 v21, 0xffff0000, v46
	v_lshl_add_u64 v[18:19], v[18:19], 0, s[10:11]
	v_pk_fma_f32 v[10:11], v[10:11], v[84:85], v[20:21]
	v_cvt_pk_bf16_f32 v0, v10, v11
	s_waitcnt vmcnt(55)
	global_store_dword v[18:19], v0, off
	v_lshlrev_b32_e32 v20, 16, v47
	v_and_b32_e32 v21, 0xffff0000, v47
	v_lshl_add_u64 v[18:19], v[18:19], 0, s[10:11]
	v_pk_fma_f32 v[10:11], v[10:11], v[86:87], v[20:21]
	v_cvt_pk_bf16_f32 v0, v10, v11
	s_waitcnt vmcnt(54)
	global_store_dword v[18:19], v0, off
	v_lshlrev_b32_e32 v20, 16, v48
	v_and_b32_e32 v21, 0xffff0000, v48
	v_lshl_add_u64 v[18:19], v[18:19], 0, s[10:11]
	v_pk_fma_f32 v[10:11], v[10:11], v[88:89], v[20:21]
	v_cvt_pk_bf16_f32 v0, v10, v11
	s_waitcnt vmcnt(53)
	global_store_dword v[18:19], v0, off
	v_lshlrev_b32_e32 v20, 16, v49
	v_and_b32_e32 v21, 0xffff0000, v49
	v_lshl_add_u64 v[18:19], v[18:19], 0, s[10:11]
	v_pk_fma_f32 v[10:11], v[10:11], v[90:91], v[20:21]
	v_cvt_pk_bf16_f32 v0, v10, v11
	s_waitcnt vmcnt(52)
	global_store_dword v[18:19], v0, off
	v_lshlrev_b32_e32 v20, 16, v50
	v_and_b32_e32 v21, 0xffff0000, v50
	v_lshl_add_u64 v[18:19], v[18:19], 0, s[10:11]
	v_pk_fma_f32 v[10:11], v[10:11], v[92:93], v[20:21]
	v_cvt_pk_bf16_f32 v0, v10, v11
	s_waitcnt vmcnt(51)
	global_store_dword v[18:19], v0, off
	v_lshlrev_b32_e32 v20, 16, v51
	v_and_b32_e32 v21, 0xffff0000, v51
	v_lshl_add_u64 v[18:19], v[18:19], 0, s[10:11]
	v_pk_fma_f32 v[10:11], v[10:11], v[94:95], v[20:21]
	v_cvt_pk_bf16_f32 v0, v10, v11
	s_waitcnt vmcnt(50)
	global_store_dword v[18:19], v0, off
	v_lshlrev_b32_e32 v20, 16, v52
	v_and_b32_e32 v21, 0xffff0000, v52
	v_lshl_add_u64 v[18:19], v[18:19], 0, s[10:11]
	v_pk_fma_f32 v[10:11], v[10:11], v[96:97], v[20:21]
	v_cvt_pk_bf16_f32 v0, v10, v11
	s_waitcnt vmcnt(49)
	global_store_dword v[18:19], v0, off
	v_lshlrev_b32_e32 v20, 16, v53
	v_and_b32_e32 v21, 0xffff0000, v53
	v_lshl_add_u64 v[18:19], v[18:19], 0, s[10:11]
	v_pk_fma_f32 v[10:11], v[10:11], v[98:99], v[20:21]
	v_cvt_pk_bf16_f32 v0, v10, v11
	s_waitcnt vmcnt(48)
	global_store_dword v[18:19], v0, off
	v_lshlrev_b32_e32 v20, 16, v54
	v_and_b32_e32 v21, 0xffff0000, v54
	v_lshl_add_u64 v[18:19], v[18:19], 0, s[10:11]
	v_pk_fma_f32 v[10:11], v[10:11], v[100:101], v[20:21]
	v_cvt_pk_bf16_f32 v0, v10, v11
	s_waitcnt vmcnt(47)
	global_store_dword v[18:19], v0, off
	v_lshlrev_b32_e32 v20, 16, v55
	v_and_b32_e32 v21, 0xffff0000, v55
	v_lshl_add_u64 v[18:19], v[18:19], 0, s[10:11]
	v_pk_fma_f32 v[10:11], v[10:11], v[102:103], v[20:21]
	v_cvt_pk_bf16_f32 v0, v10, v11
	s_waitcnt vmcnt(46)
	global_store_dword v[18:19], v0, off
	v_lshlrev_b32_e32 v20, 16, v56
	v_and_b32_e32 v21, 0xffff0000, v56
	v_lshl_add_u64 v[18:19], v[18:19], 0, s[10:11]
	v_pk_fma_f32 v[10:11], v[10:11], v[104:105], v[20:21]
	v_cvt_pk_bf16_f32 v0, v10, v11
	s_waitcnt vmcnt(45)
; #define GAS __attribute__((address_space(1)))
; #define SB() __builtin_amdgcn_sched_barrier(0)
; __device__ __forceinline__ unsigned cvt_pk_bf16(float lo, float hi) { unsigned r; asm volatile("v_cvt_pk_bf16_f32 %0, %1, %2" : "=v"(r) : "v"(lo), "v"(hi)); return r; }
; __device__ __forceinline__ float bflo(unsigned w) { return __uint_as_float(w << 16); }
; __device__ __forceinline__ float bfhi(unsigned w) { return __uint_as_float(w & 0xffff0000u); }
; __device__ __forceinline__ void hg_scan_item(Frame& F, int B) {
;     ...
;     for (int c0 = 0; c0 < 32; c0 += 8) { unsigned u[8]; f32x2 gg[8];
; #pragma unroll
;         for (int i = 0; i < 8; ++i) { u[i] = ut[(size_t)(c0 + i) * 8192]; gg[i] = *(const GAS f32x2*)(gd + (c0 + i) * 128); }
;         SB();
; #pragma unroll
;         for (int i = 0; i < 8; ++i) { sp[(size_t)(c0 + i) * 8192] = cvt_pk_bf16(s0, s1); s0 = gg[i].x * s0 + bflo(u[i]); s1 = gg[i].y * s1 + bfhi(u[i]); } }
; __global__ void __launch_bounds__(NTHR, 2) mega_fwd(Args args) {
;     ...
;                     for (int B = bx - sc0; B < 256; B += nsc) hg_scan_item(F, B);
	global_store_dword v[18:19], v0, off
	v_lshlrev_b32_e32 v20, 16, v57
	v_and_b32_e32 v21, 0xffff0000, v57
	v_lshl_add_u64 v[18:19], v[18:19], 0, s[10:11]
	v_pk_fma_f32 v[10:11], v[10:11], v[106:107], v[20:21]
	v_cvt_pk_bf16_f32 v0, v10, v11
	s_waitcnt vmcnt(44)
	global_store_dword v[18:19], v0, off
	v_lshlrev_b32_e32 v20, 16, v58
	v_and_b32_e32 v21, 0xffff0000, v58
	v_lshl_add_u64 v[18:19], v[18:19], 0, s[10:11]
	v_pk_fma_f32 v[10:11], v[10:11], v[108:109], v[20:21]
	v_cvt_pk_bf16_f32 v0, v10, v11
	s_waitcnt vmcnt(43)
	global_store_dword v[18:19], v0, off
	v_lshlrev_b32_e32 v20, 16, v59
	v_and_b32_e32 v21, 0xffff0000, v59
	v_lshl_add_u64 v[18:19], v[18:19], 0, s[10:11]
	v_pk_fma_f32 v[10:11], v[10:11], v[110:111], v[20:21]
	v_cvt_pk_bf16_f32 v0, v10, v11
	s_waitcnt vmcnt(42)
	global_store_dword v[18:19], v0, off
	v_lshlrev_b32_e32 v20, 16, v60
	v_and_b32_e32 v21, 0xffff0000, v60
	v_lshl_add_u64 v[18:19], v[18:19], 0, s[10:11]
	v_pk_fma_f32 v[10:11], v[10:11], v[112:113], v[20:21]
	v_cvt_pk_bf16_f32 v0, v10, v11
	s_waitcnt vmcnt(41)
	global_store_dword v[18:19], v0, off
	v_lshlrev_b32_e32 v20, 16, v61
	v_and_b32_e32 v21, 0xffff0000, v61
	v_lshl_add_u64 v[18:19], v[18:19], 0, s[10:11]
	v_pk_fma_f32 v[10:11], v[10:11], v[114:115], v[20:21]
	v_cvt_pk_bf16_f32 v0, v10, v11
	s_waitcnt vmcnt(40)
	global_store_dword v[18:19], v0, off
	v_lshlrev_b32_e32 v20, 16, v62
	v_and_b32_e32 v21, 0xffff0000, v62
	v_lshl_add_u64 v[18:19], v[18:19], 0, s[10:11]
	v_pk_fma_f32 v[10:11], v[10:11], v[116:117], v[20:21]
	v_cvt_pk_bf16_f32 v0, v10, v11
	s_waitcnt vmcnt(39)
	global_store_dword v[18:19], v0, off
	v_lshlrev_b32_e32 v20, 16, v63
	v_and_b32_e32 v21, 0xffff0000, v63
	v_lshl_add_u64 v[18:19], v[18:19], 0, s[10:11]
	v_pk_fma_f32 v[10:11], v[10:11], v[118:119], v[20:21]
	v_cvt_pk_bf16_f32 v0, v10, v11
	s_waitcnt vmcnt(38)
	global_store_dword v[18:19], v0, off
	v_lshlrev_b32_e32 v20, 16, v64
	v_and_b32_e32 v21, 0xffff0000, v64
	v_lshl_add_u64 v[18:19], v[18:19], 0, s[10:11]
	v_pk_fma_f32 v[10:11], v[10:11], v[120:121], v[20:21]
	v_cvt_pk_bf16_f32 v0, v10, v11
	s_waitcnt vmcnt(37)
	global_store_dword v[18:19], v0, off
	v_lshlrev_b32_e32 v20, 16, v65
	v_and_b32_e32 v21, 0xffff0000, v65
	v_lshl_add_u64 v[18:19], v[18:19], 0, s[10:11]
	v_pk_fma_f32 v[10:11], v[10:11], v[122:123], v[20:21]
	v_cvt_pk_bf16_f32 v0, v10, v11
	s_waitcnt vmcnt(36)
	global_store_dword v[18:19], v0, off
	v_lshlrev_b32_e32 v20, 16, v66
	v_and_b32_e32 v21, 0xffff0000, v66
	v_lshl_add_u64 v[18:19], v[18:19], 0, s[10:11]
	v_pk_fma_f32 v[10:11], v[10:11], v[124:125], v[20:21]
	v_cvt_pk_bf16_f32 v0, v10, v11
	s_waitcnt vmcnt(35)
	global_store_dword v[18:19], v0, off
	v_lshlrev_b32_e32 v20, 16, v67
	v_and_b32_e32 v21, 0xffff0000, v67
	v_lshl_add_u64 v[18:19], v[18:19], 0, s[10:11]
	v_pk_fma_f32 v[10:11], v[10:11], v[126:127], v[20:21]
	v_cvt_pk_bf16_f32 v0, v10, v11
	s_waitcnt vmcnt(34)
	global_store_dword v[18:19], v0, off
	v_lshlrev_b32_e32 v20, 16, v68
	v_and_b32_e32 v21, 0xffff0000, v68
	v_lshl_add_u64 v[18:19], v[18:19], 0, s[10:11]
	v_pk_fma_f32 v[10:11], v[10:11], v[128:129], v[20:21]
	v_cvt_pk_bf16_f32 v0, v10, v11
	s_waitcnt vmcnt(33)
	global_store_dword v[18:19], v0, off
	v_lshlrev_b32_e32 v20, 16, v69
	v_and_b32_e32 v21, 0xffff0000, v69
	v_lshl_add_u64 v[18:19], v[18:19], 0, s[10:11]
	v_pk_fma_f32 v[10:11], v[10:11], v[130:131], v[20:21]
	v_cvt_pk_bf16_f32 v0, v10, v11
	s_waitcnt vmcnt(32)
	global_store_dword v[18:19], v0, off
	v_lshlrev_b32_e32 v20, 16, v70
	v_and_b32_e32 v21, 0xffff0000, v70
	v_lshl_add_u64 v[18:19], v[18:19], 0, s[10:11]
	v_pk_fma_f32 v[10:11], v[10:11], v[132:133], v[20:21]
	v_cvt_pk_bf16_f32 v0, v10, v11
	s_waitcnt vmcnt(31)
	global_store_dword v[18:19], v0, off
	v_lshlrev_b32_e32 v20, 16, v71
	v_and_b32_e32 v21, 0xffff0000, v71
	v_pk_fma_f32 v[10:11], v[10:11], v[134:135], v[20:21]
	v_readlane_b32 s8, v249, 44
	s_add_i32 s7, s7, s8
	s_add_i32 s6, s6, s13
	s_cmpk_gt_i32 s7, 0xff
	s_cbranch_scc0 .LBB0_777
